# v24
# baseline (speedup 1.0000x reference)
.LBB0_4:
	s_or_b64 exec, exec, s[6:7]
	s_load_dwordx2 s[6:7], s[0:1], 0x28
	s_mov_b32 s34, 0
	v_cmp_eq_u32_e64 s[0:1], 0, v0
	v_lshlrev_b32_e32 v1, 2, v131
	v_or_b32_e32 v2, 0x22200, v1
	v_or_b32_e32 v3, 0x22300, v1
	s_waitcnt lgkmcnt(0)
	s_barrier
	ds_read_b32 v2, v2
	ds_read_b32 v3, v3
	v_and_b32_e32 v202, 15, v0
	s_lshl_b32 s30, s31, 4
	v_or_b32_e32 v132, s30, v202
	s_waitcnt lgkmcnt(0)
	v_add_f32_e32 v2, v2, v3
	v_mbcnt_lo_u32_b32 v3, -1, 0
	v_mbcnt_hi_u32_b32 v3, -1, v3
	v_and_b32_e32 v4, 64, v3
	v_add_u32_e32 v4, 64, v4
	v_xor_b32_e32 v5, 32, v3
	v_cmp_lt_i32_e32 vcc, v5, v4
	v_mov_b32_e32 v133, 0
	v_lshrrev_b32_e32 v209, 4, v131
	v_cndmask_b32_e32 v5, v3, v5, vcc
	v_lshlrev_b32_e32 v200, 2, v5
	v_and_b32_e32 v203, 48, v0
	v_xor_b32_e32 v5, 16, v3
	v_cmp_lt_i32_e32 vcc, v5, v4
	v_cndmask_b32_e32 v5, v3, v5, vcc
	v_lshlrev_b32_e32 v201, 2, v5
	v_xor_b32_e32 v5, 8, v3
	v_cmp_lt_i32_e32 vcc, v5, v4
	v_cndmask_b32_e32 v5, v3, v5, vcc
	v_lshlrev_b32_e32 v205, 2, v5
	v_cmp_eq_u32_e64 s[8:9], 0, v131
	v_mov_b32_e32 v218, 0xff800000
	v_mov_b32_e32 v213, 0x23420
	v_xor_b32_e32 v5, 4, v3
	v_cmp_lt_i32_e32 vcc, v5, v4
	v_cndmask_b32_e32 v5, v3, v5, vcc
	v_lshlrev_b32_e32 v206, 2, v5
	v_xor_b32_e32 v5, 2, v3
	v_cmp_lt_i32_e32 vcc, v5, v4
	v_mov_b32_e32 v219, 0
	s_mov_b32 s35, s31
	v_cndmask_b32_e32 v5, v3, v5, vcc
	v_lshlrev_b32_e32 v207, 2, v5
	v_mov_b32_e32 v138, 0
	v_mov_b32_e32 v139, v133
	v_mov_b32_e32 v136, 0
	v_mov_b32_e32 v137, v133
	v_xor_b32_e32 v5, 1, v3
	v_cmp_lt_i32_e32 vcc, v5, v4
	v_lshlrev_b32_e32 v4, 3, v131
	v_cndmask_b32_e32 v3, v3, v5, vcc
	v_lshlrev_b32_e32 v208, 2, v3
	v_mov_b32_e32 v150, 0
	s_nop 1
	v_add_f32_dpp v2, v2, v2 row_shr:1 row_mask:0xf bank_mask:0xf
	s_nop 1
	v_add_f32_dpp v2, v2, v2 row_shr:2 row_mask:0xf bank_mask:0xf
	s_nop 1
	v_add_f32_dpp v2, v2, v2 row_shr:4 row_mask:0xf bank_mask:0xf
	s_nop 1
	v_add_f32_dpp v2, v2, v2 row_shr:8 row_mask:0xf bank_mask:0xf
	s_nop 1
	v_add_f32_dpp v2, v2, v2 row_bcast:15 row_mask:0xa bank_mask:0xf
	s_nop 1
	v_add_f32_dpp v2, v2, v2 row_bcast:31 row_mask:0xc bank_mask:0xf
	s_nop 1
	v_readlane_b32 s44, v2, 63
	s_nop 1
	v_mov_b32_e32 v2, s44
	v_add_f32_e32 v2, s43, v2
	s_mul_i32 s4, s31, 0x2200
	s_add_i32 s24, s4, 0x11000
	v_mul_f32_e32 v210, 0x3fb8aa3b, v2
	s_movk_i32 s4, 0x220
	v_mov_b32_e32 v2, s24
	v_mad_u32_u24 v5, v202, s4, v2
	v_lshlrev_b64 v[2:3], 9, v[132:133]
	v_lshl_add_u64 v[2:3], s[6:7], 0, v[2:3]
	v_lshlrev_b32_e32 v132, 5, v209
	v_add_u32_e32 v212, s24, v4
	v_mad_u32_u24 v211, v202, s4, v203
	v_lshl_add_u64 v[134:135], v[2:3], 0, v[132:133]
	v_cmp_eq_u32_e64 s[6:7], 15, v202
	v_cmp_eq_u32_e64 s[4:5], 15, v131
	v_add_u32_e32 v214, v5, v203
	v_add_u32_e32 v215, 0x800, v212
	v_add_u32_e32 v216, 0x1000, v212
	v_add_u32_e32 v217, 0x1800, v212
	v_mov_b32_e32 v151, v133
	v_mov_b32_e32 v140, 0
	v_mov_b32_e32 v141, v133
	v_mov_b32_e32 v178, 0
	v_mov_b32_e32 v179, v133
	v_mov_b32_e32 v168, 0
	v_mov_b32_e32 v169, v133
	v_mov_b32_e32 v182, 0
	v_mov_b32_e32 v183, v133
	v_mov_b32_e32 v180, 0
	v_mov_b32_e32 v181, v133
	v_mov_b32_e32 v186, 0
	v_mov_b32_e32 v187, v133
	v_mov_b32_e32 v184, 0
	v_mov_b32_e32 v185, v133
	v_mov_b32_e32 v190, 0
	v_mov_b32_e32 v191, v133
	v_mov_b32_e32 v188, 0
	v_mov_b32_e32 v189, v133
	v_mov_b32_e32 v194, 0
	v_mov_b32_e32 v195, v133
	v_mov_b32_e32 v192, 0
	v_mov_b32_e32 v193, v133
	v_mov_b32_e32 v198, 0
	v_mov_b32_e32 v199, v133
	v_mov_b32_e32 v196, 0
	v_mov_b32_e32 v197, v133
	s_cmp_eq_u32 s2, 0
	s_cselect_b64 s[24:25], -1, 0
	s_and_b64 s[24:25], s[24:25], s[10:11]
	s_and_saveexec_b64 s[26:27], s[24:25]
	s_cbranch_execz .Lp1_noinit
	global_store_dword v[254:255], v253, off
